# XCD-local barriers: the merge->out, out->router-pass and FFN-up->FFN-down barriers have XCD-local dependencies, so their leaders skip the L2 write-back and the cross-XCD top-level handshake (runtime c
# speedup vs baseline: 1.0144x; 1.0110x over previous
_Z6mk_fwd4Args:
	s_load_dword s10, s[0:1], 0x90
	s_mov_b32 s11, s2
	s_add_u32 s2, s0, 0x90
	s_addc_u32 s3, s1, 0
	v_lshl_add_u32 v1, v0, 2, 0
	v_writelane_b32 v253, s2, 0
	v_add_u32_e32 v1, 0x20000, v1
	v_mov_b32_e32 v2, 0
	v_readfirstlane_b32 s22, v0
	v_writelane_b32 v253, s3, 1
	ds_write2st64_b32 v1, v2, v2 offset1:8
	ds_write2st64_b32 v1, v2, v2 offset0:16 offset1:24
	v_or_b32_e32 v1, 0x800, v0
	s_mov_b64 s[2:3], -1
	s_and_saveexec_b64 s[4:5], s[2:3]
	v_lshl_add_u32 v3, v1, 2, 0
	v_add_u32_e32 v3, 0x20000, v3
	ds_write_b32 v3, v2
	s_or_b64 exec, exec, s[4:5]
	s_and_saveexec_b64 s[4:5], s[2:3]
	s_add_i32 s2, 0, 0x20000
	v_lshl_add_u32 v1, v1, 2, s2
	v_mov_b32_e32 v2, 0
	ds_write_b32 v1, v2 offset:2048
	s_or_b64 exec, exec, s[4:5]
	v_or_b32_e32 v1, 0xc00, v0
	v_cmp_gt_u32_e64 s[2:3], 7, 6
	v_cmp_gt_u32_e64 s[6:7], 7, 5
	s_and_saveexec_b64 s[4:5], s[6:7]
	v_lshl_add_u32 v2, v1, 2, 0
	v_add_u32_e32 v2, 0x20000, v2
	v_mov_b32_e32 v3, 0
	ds_write_b32 v2, v3
	s_or_b64 exec, exec, s[4:5]
	s_load_dwordx16 s[48:63], s[0:1], 0x40
	s_and_saveexec_b64 s[4:5], s[2:3]
	s_add_i32 s2, 0, 0x20000
	v_lshl_add_u32 v1, v1, 2, s2
	v_mov_b32_e32 v2, 0
	ds_write_b32 v1, v2 offset:2048
	s_or_b64 exec, exec, s[4:5]
	s_waitcnt lgkmcnt(0)
	s_add_u32 s2, s62, 0x4000
	s_addc_u32 s3, s63, 0
	v_writelane_b32 v253, s2, 2
	s_barrier
	s_nop 0
	v_writelane_b32 v253, s3, 3
	s_getreg_b32 s6, hwreg(HW_REG_XCC_ID, 0, 4)
	v_cmp_eq_u32_e64 s[4:5], 0, v0
	s_mov_b64 s[2:3], exec
	s_nop 0
	v_writelane_b32 v253, s4, 4
	s_nop 1
	v_writelane_b32 v253, s5, 5
	s_and_b64 s[4:5], s[2:3], s[4:5]
	s_mov_b64 exec, s[4:5]
	s_cbranch_execz .LBB0_11
	s_mov_b64 s[4:5], exec
	v_mbcnt_lo_u32_b32 v1, s4, 0
	v_mbcnt_hi_u32_b32 v1, s5, v1
	v_cmp_eq_u32_e32 vcc, 0, v1
	s_and_b64 s[8:9], exec, vcc
	s_mov_b64 exec, s[8:9]
	s_cbranch_execz .LBB0_11
	s_lshl_b32 s6, s6, 8
	s_bcnt1_i32_b64 s4, s[4:5]
	s_and_b32 s6, s6, 0xf00
	v_mov_b32_e32 v2, s4
	v_readlane_b32 s4, v253, 2
	v_mov_b32_e32 v1, s6
	v_readlane_b32 s5, v253, 3
	s_nop 4
	global_atomic_add v1, v2, s[4:5] offset:1024
	s_lshr_b32 s6, s6, 8
	s_and_b32 s7, s11, 7
	s_cmp_eq_u32 s6, s7
	s_cbranch_scc1 .Lmm_ok
	v_mov_b32_e32 v1, 0x300
	s_nop 0
	global_atomic_add v1, v2, s[4:5]
.Lmm_ok:
.LBB0_11:
	s_or_b64 exec, exec, s[2:3]
	v_mov_b32_e32 v1, v0
	s_mov_b64 s[2:3], 0
	s_mov_b32 s24, s11
	s_mov_b32 s23, s10
	s_nop 0
	v_writelane_b32 v253, s2, 6
	s_nop 1
	v_writelane_b32 v253, s3, 7
	s_and_b32 s2, s23, 7
	s_cmp_lg_u32 s2, 0
	s_cbranch_scc1 .LBB0_13
	s_ashr_i32 s3, s24, 31
	s_lshr_b32 s3, s3, 29
	s_add_i32 s3, s24, s3
	s_ashr_i32 s4, s3, 3
	s_and_b32 s3, s3, -8
	s_ashr_i32 s2, s23, 3
	s_sub_i32 s3, s24, s3
	s_mul_i32 s2, s3, s2
	s_add_i32 s24, s2, s4

.LBB0_607:
	s_mov_b64 s[2:3], exec
	s_lshl_b32 s0, s37, 8
	v_readlane_b32 s4, v253, 2
	v_mbcnt_lo_u32_b32 v3, s2, 0
	v_readlane_b32 s5, v253, 3
	s_add_u32 s0, s4, s0
	v_mbcnt_hi_u32_b32 v3, s3, v3
	s_addc_u32 s1, s5, 0
	v_mov_b32_e32 v21, 0x300
	s_nop 4
	global_load_dword v20, v21, s[4:5] sc1
	v_cmp_eq_u32_e32 vcc, 0, v3
	s_and_saveexec_b64 s[4:5], vcc
	s_cbranch_execz .LBB0_609
	s_bcnt1_i32_b64 s2, s[2:3]
	v_mov_b32_e32 v5, s2
	v_mov_b32_e32 v6, 0x1000
	global_atomic_add v5, v6, v5, s[0:1] offset:1024 sc0

.LBB0_623:
	s_andn2_saveexec_b64 s[2:3], s[2:3]
	s_cbranch_execz .LBB0_643
	s_mov_b64 s[4:5], exec
	v_cmp_eq_u32_e32 vcc, 0, v20
	s_cbranch_vccnz .Lxl_2
	buffer_wbl2 sc1
	s_waitcnt lgkmcnt(0)
	s_waitcnt vmcnt(0)
	v_mbcnt_lo_u32_b32 v3, s4, 0
	v_mbcnt_hi_u32_b32 v3, s5, v3
	v_cmp_eq_u32_e32 vcc, 0, v3
	s_and_saveexec_b64 s[6:7], vcc
	s_cbranch_execz .LBB0_626
	s_bcnt1_i32_b64 s4, s[4:5]
	v_mov_b32_e32 v4, s4
	v_readlane_b32 s4, v253, 30
	v_readlane_b32 s5, v253, 31
	s_nop 4
	global_atomic_add v4, v195, v4, s[4:5] sc0

.Lxl_2:
	s_mov_b64 s[4:5], exec
	v_mbcnt_lo_u32_b32 v2, s4, 0
	v_mbcnt_hi_u32_b32 v2, s5, v2
	v_cmp_eq_u32_e32 vcc, 0, v2
	s_waitcnt vmcnt(0)
	s_and_saveexec_b64 s[6:7], vcc
	s_cbranch_execz .LBB0_642
	s_bcnt1_i32_b64 s4, s[4:5]
	v_mov_b32_e32 v2, s4
	v_mov_b32_e32 v3, 0x2000
	global_atomic_add v3, v2, s[0:1] offset:1024

.LBB0_707:
	s_andn2_saveexec_b64 s[2:3], s[2:3]
	s_cbranch_execz .LBB0_727
	s_mov_b64 s[2:3], exec
	v_cmp_eq_u32_e32 vcc, 0, v20
	s_cbranch_vccnz .Lxl_1
	buffer_wbl2 sc1
	s_waitcnt lgkmcnt(0)
	s_waitcnt vmcnt(0)
	v_mbcnt_lo_u32_b32 v3, s2, 0
	v_mbcnt_hi_u32_b32 v3, s3, v3
	v_cmp_eq_u32_e32 vcc, 0, v3
	s_and_saveexec_b64 s[4:5], vcc
	s_cbranch_execz .LBB0_710
	s_bcnt1_i32_b64 s2, s[2:3]
	v_mov_b32_e32 v4, s2
	v_readlane_b32 s2, v253, 30
	v_readlane_b32 s3, v253, 31
	s_nop 4
	global_atomic_add v4, v195, v4, s[2:3] sc0

.Lxl_1:
	s_mov_b64 s[2:3], exec
	v_mbcnt_lo_u32_b32 v2, s2, 0
	v_mbcnt_hi_u32_b32 v2, s3, v2
	v_cmp_eq_u32_e32 vcc, 0, v2
	s_waitcnt vmcnt(0)
	s_and_saveexec_b64 s[4:5], vcc
	s_cbranch_execz .LBB0_726
	s_bcnt1_i32_b64 s2, s[2:3]
	v_mov_b32_e32 v2, s2
	v_mov_b32_e32 v3, 0x2000
	global_atomic_add v3, v2, s[0:1] offset:1024

.LBB0_989:
	s_mov_b64 s[2:3], exec
	s_lshl_b32 s0, s36, 8
	v_readlane_b32 s4, v253, 2
	v_mbcnt_lo_u32_b32 v3, s2, 0
	v_readlane_b32 s5, v253, 3
	s_add_u32 s0, s4, s0
	v_mbcnt_hi_u32_b32 v3, s3, v3
	s_addc_u32 s1, s5, 0
	v_mov_b32_e32 v21, 0x300
	s_nop 4
	global_load_dword v20, v21, s[4:5] sc1
	v_cmp_eq_u32_e32 vcc, 0, v3
	s_and_saveexec_b64 s[4:5], vcc
	s_cbranch_execz .LBB0_991
	s_bcnt1_i32_b64 s2, s[2:3]
	v_mov_b32_e32 v5, s2
	v_mov_b32_e32 v6, 0x1000
	global_atomic_add v5, v6, v5, s[0:1] offset:1024 sc0
